# v47 + adaLN GEMV partial items 2048..3071 dealt to waves 0-3 of every workgroup (was: all waves of workgroups 0-127)
# speedup vs baseline: 1.0046x; 1.0046x over previous
; #define GAS __attribute__((address_space(1)))
; #define LAS __attribute__((address_space(3)))
; __device__ __forceinline__ void ada_item(const float* wada, float* adap, const LAS float* S, int it, int lane) {
;     const int l = it / 1536, rem = it - l * 1536, cg = rem >> 5, ks = rem & 31; const int k0 = ks * 64, col = cg * 256 + 4 * lane;
;     const float* w = wada + ((size_t)l * D + k0) * ADAW + col;
;     f32x4 a0 = {0.f, 0.f, 0.f, 0.f}, a1 = a0, a2 = a0;
; #pragma unroll 8
;     for (int kk = 0; kk < 64; ++kk) { const f32x4 v = *(const GAS f32x4*)(w + (size_t)kk * ADAW); const float s0 = S[k0 + kk], s1 = S[2048 + k0 + kk], s2 = S[4096 + k0 + kk];
;         a0 += v * s0; a1 += v * s1; a2 += v * s2; }
;     float* o = adap + (((size_t)l * 32 + ks) * 3) * ADAW + col;
;     *(GAS f32x4*)o = a0; *(GAS f32x4*)(o + ADAW) = a1; *(GAS f32x4*)(o + 2 * ADAW) = a2;
; }
; __device__ __forceinline__ void p0a_phase(KA A, LAS unsigned char* lds, int tid, int wave, int lane, int bid, int G) {
;     ...
;     const int gw = bid * NWAVES + wave, NGW = G * NWAVES;
;     for (int it = gw; it < 3072; it += NGW) ada_item(A->in[I_WADA], (float*)(ws + WS_ADAP), S, it, lane);
.LBB0_63:
	v_add_co_u32_e64 v52, s[4:5], s22, v14
	v_add_co_u32_e32 v50, vcc, 0xfffd0000, v14
	s_nop 0
	v_addc_co_u32_e64 v53, s[4:5], -1, v15, s[4:5]
	v_add_co_u32_e64 v54, s[4:5], s23, v14
	global_load_dwordx4 v[18:21], v[14:15], off
	s_nop 0
	v_addc_co_u32_e64 v55, s[4:5], -1, v15, s[4:5]
	v_add_co_u32_e64 v56, s[4:5], s24, v14
	v_addc_co_u32_e32 v51, vcc, -1, v15, vcc
	s_nop 0
	v_addc_co_u32_e64 v57, s[4:5], -1, v15, s[4:5]
	v_add_co_u32_e64 v58, s[4:5], s25, v14
	s_nop 1
	v_addc_co_u32_e64 v59, s[4:5], 0, v15, s[4:5]
	v_add_co_u32_e64 v60, s[4:5], s26, v14
	s_nop 1
	v_addc_co_u32_e64 v61, s[4:5], 0, v15, s[4:5]
	v_add_co_u32_e64 v62, s[4:5], s27, v14
	s_nop 1
	v_addc_co_u32_e64 v63, s[4:5], 0, v15, s[4:5]
	global_load_dwordx4 v[22:25], v[52:53], off
	global_load_dwordx4 v[26:29], v[54:55], off
	global_load_dwordx4 v[30:33], v[56:57], off
	global_load_dwordx4 v[34:37], v[58:59], off
	global_load_dwordx4 v[38:41], v[50:51], off
	global_load_dwordx4 v[42:45], v[60:61], off
	global_load_dwordx4 v[46:49], v[62:63], off
	s_add_i32 s4, s29, s30
	s_add_i32 s5, s4, 0x12000
	s_add_i32 s31, s4, 0x14000
	s_add_i32 s33, s4, 0x16000
	s_add_i32 s34, s4, 0x12010
	s_add_i32 s35, s4, 0x14010
	s_add_i32 s4, s4, 0x16010
	v_mov_b32_e32 v17, s5
	v_mov_b32_e32 v54, s31
	v_mov_b32_e32 v58, s33
	v_mov_b32_e32 v62, s34
	v_mov_b32_e32 v66, s35
	v_mov_b32_e32 v70, s4
	ds_read_b128 v[50:53], v17
	ds_read_b128 v[54:57], v54
	ds_read_b128 v[58:61], v58
	ds_read_b128 v[62:65], v62
	ds_read_b128 v[66:69], v66
	ds_read_b128 v[70:73], v70
	s_waitcnt lgkmcnt(5)
	v_mov_b32_e32 v74, v53
	s_waitcnt lgkmcnt(4)
	v_mov_b32_e32 v76, v57
	s_waitcnt lgkmcnt(3)
	v_mov_b32_e32 v78, v61
	s_add_i32 s30, s30, 32
	s_waitcnt lgkmcnt(2)
	v_mov_b32_e32 v80, v65
	s_waitcnt lgkmcnt(1)
	v_mov_b32_e32 v84, v69
	s_waitcnt lgkmcnt(0)
	v_mov_b32_e32 v86, v73
	v_lshl_add_u64 v[14:15], v[14:15], 0, s[10:11]
	s_cmpk_lg_i32 s30, 0x100
	s_waitcnt vmcnt(2)
	v_pk_fma_f32 v[8:9], v[40:41], v[50:51], v[8:9] op_sel_hi:[1,0,1]
	v_pk_fma_f32 v[6:7], v[38:39], v[50:51], v[6:7] op_sel_hi:[1,0,1]
	v_pk_fma_f32 v[12:13], v[40:41], v[54:55], v[12:13] op_sel_hi:[1,0,1]
	v_pk_fma_f32 v[10:11], v[38:39], v[54:55], v[10:11] op_sel_hi:[1,0,1]
	v_pk_fma_f32 v[4:5], v[40:41], v[58:59], v[4:5] op_sel_hi:[1,0,1]
	v_pk_fma_f32 v[2:3], v[38:39], v[58:59], v[2:3] op_sel_hi:[1,0,1]
	v_pk_fma_f32 v[8:9], v[24:25], v[50:51], v[8:9] op_sel:[0,1,0]
	v_pk_fma_f32 v[6:7], v[22:23], v[50:51], v[6:7] op_sel:[0,1,0]
	v_pk_fma_f32 v[12:13], v[24:25], v[54:55], v[12:13] op_sel:[0,1,0]
	v_pk_fma_f32 v[10:11], v[22:23], v[54:55], v[10:11] op_sel:[0,1,0]
	v_pk_fma_f32 v[4:5], v[24:25], v[58:59], v[4:5] op_sel:[0,1,0]
	v_pk_fma_f32 v[2:3], v[22:23], v[58:59], v[2:3] op_sel:[0,1,0]
	v_pk_fma_f32 v[8:9], v[28:29], v[52:53], v[8:9] op_sel_hi:[1,0,1]
	v_pk_fma_f32 v[6:7], v[26:27], v[52:53], v[6:7] op_sel_hi:[1,0,1]
	v_pk_fma_f32 v[12:13], v[28:29], v[56:57], v[12:13] op_sel_hi:[1,0,1]
	v_pk_fma_f32 v[10:11], v[26:27], v[56:57], v[10:11] op_sel_hi:[1,0,1]
	v_pk_fma_f32 v[4:5], v[28:29], v[60:61], v[4:5] op_sel_hi:[1,0,1]
	v_pk_fma_f32 v[2:3], v[26:27], v[60:61], v[2:3] op_sel_hi:[1,0,1]
	v_pk_fma_f32 v[8:9], v[32:33], v[74:75], v[8:9] op_sel_hi:[1,0,1]
	v_pk_fma_f32 v[6:7], v[30:31], v[74:75], v[6:7] op_sel_hi:[1,0,1]
	v_pk_fma_f32 v[12:13], v[32:33], v[76:77], v[12:13] op_sel_hi:[1,0,1]
	v_pk_fma_f32 v[10:11], v[30:31], v[76:77], v[10:11] op_sel_hi:[1,0,1]
	v_pk_fma_f32 v[4:5], v[32:33], v[78:79], v[4:5] op_sel_hi:[1,0,1]
	v_pk_fma_f32 v[2:3], v[30:31], v[78:79], v[2:3] op_sel_hi:[1,0,1]
	v_pk_fma_f32 v[8:9], v[20:21], v[62:63], v[8:9] op_sel_hi:[1,0,1]
	v_pk_fma_f32 v[6:7], v[18:19], v[62:63], v[6:7] op_sel_hi:[1,0,1]
	v_pk_fma_f32 v[12:13], v[20:21], v[66:67], v[12:13] op_sel_hi:[1,0,1]
	v_pk_fma_f32 v[10:11], v[18:19], v[66:67], v[10:11] op_sel_hi:[1,0,1]
	v_pk_fma_f32 v[4:5], v[20:21], v[70:71], v[4:5] op_sel_hi:[1,0,1]
	v_pk_fma_f32 v[2:3], v[18:19], v[70:71], v[2:3] op_sel_hi:[1,0,1]
	v_pk_fma_f32 v[8:9], v[36:37], v[62:63], v[8:9] op_sel:[0,1,0]
	v_pk_fma_f32 v[6:7], v[34:35], v[62:63], v[6:7] op_sel:[0,1,0]
	v_pk_fma_f32 v[12:13], v[36:37], v[66:67], v[12:13] op_sel:[0,1,0]
	v_pk_fma_f32 v[10:11], v[34:35], v[66:67], v[10:11] op_sel:[0,1,0]
	v_pk_fma_f32 v[4:5], v[36:37], v[70:71], v[4:5] op_sel:[0,1,0]
	v_pk_fma_f32 v[2:3], v[34:35], v[70:71], v[2:3] op_sel:[0,1,0]
	s_waitcnt vmcnt(1)
	v_pk_fma_f32 v[8:9], v[44:45], v[64:65], v[8:9] op_sel_hi:[1,0,1]
	v_pk_fma_f32 v[6:7], v[42:43], v[64:65], v[6:7] op_sel_hi:[1,0,1]
	v_pk_fma_f32 v[12:13], v[44:45], v[68:69], v[12:13] op_sel_hi:[1,0,1]
	v_pk_fma_f32 v[10:11], v[42:43], v[68:69], v[10:11] op_sel_hi:[1,0,1]
	v_pk_fma_f32 v[4:5], v[44:45], v[72:73], v[4:5] op_sel_hi:[1,0,1]
	v_pk_fma_f32 v[2:3], v[42:43], v[72:73], v[2:3] op_sel_hi:[1,0,1]
	s_waitcnt vmcnt(0)
	v_pk_fma_f32 v[8:9], v[48:49], v[80:81], v[8:9] op_sel_hi:[1,0,1]
	v_pk_fma_f32 v[6:7], v[46:47], v[80:81], v[6:7] op_sel_hi:[1,0,1]
	v_pk_fma_f32 v[12:13], v[48:49], v[84:85], v[12:13] op_sel_hi:[1,0,1]
	v_pk_fma_f32 v[10:11], v[46:47], v[84:85], v[10:11] op_sel_hi:[1,0,1]
	v_pk_fma_f32 v[4:5], v[48:49], v[86:87], v[4:5] op_sel_hi:[1,0,1]
	v_pk_fma_f32 v[2:3], v[46:47], v[86:87], v[2:3] op_sel_hi:[1,0,1]
	s_cbranch_scc1 .LBB0_63
	s_mul_i32 s4, s28, 0xfffffa00
	s_add_i32 s4, s4, s12
	s_lshl_b32 s4, s4, 3
	s_and_b32 s4, s4, 0xffffff00
	s_and_b32 s5, s12, 31
	v_or_b32_e32 v14, s4, v16
	s_lshl_b32 s4, s28, 5
	s_or_b32 s4, s4, s5
	s_mul_hi_i32 s5, s4, 0x24000
	s_mul_i32 s4, s4, 0x24000
	s_add_u32 s4, s14, s4
	v_ashrrev_i32_e32 v15, 31, v14
	s_addc_u32 s5, s16, s5
	v_lshl_add_u64 v[14:15], v[14:15], 2, s[4:5]
	global_store_dwordx4 v[14:15], v[6:9], off
	s_add_i32 s12, s12, s13
	s_add_i32 s17, s17, s13
	v_add_co_u32_e32 v6, vcc, 0xc000, v14
	s_add_i32 s20, s20, s21
	s_nop 0
	v_addc_co_u32_e32 v7, vcc, 0, v15, vcc
	global_store_dwordx4 v[6:7], v[10:13], off
	v_add_co_u32_e32 v6, vcc, 0x18000, v14
	s_sub_i32 s100, s12, 0x800
	s_lshr_b32 s101, s100, 3
	s_lshl_b32 s101, s101, 2
	s_and_b32 s12, s100, 3
	s_add_i32 s12, s12, s101
	s_addk_i32 s12, 0x800
	s_and_b32 s100, s100, 4
	s_cmp_lg_u32 s100, 0
	s_cselect_b32 s12, 0x1000, s12
	s_mov_b32 s17, s12
	s_lshl_b32 s20, s12, 3
	s_cmpk_gt_i32 s12, 0xbff
	s_nop 0
	v_addc_co_u32_e32 v7, vcc, 0, v15, vcc
	global_store_dwordx4 v[6:7], v[2:5], off
	s_cbranch_scc0 .LBB0_62
